# baseline (speedup 1.0000x reference)
.LBB1_3:
	v_lshlrev_b32_e32 v34, 5, v208
	v_lshlrev_b32_e32 v203, 2, v201
	v_lshrrev_b32_e32 v35, 2, v0
	v_and_b32_e32 v191, 32, v34
	v_and_or_b32 v35, v35, 3, v203
	v_add_u32_e32 v34, s30, v191
	v_lshlrev_b32_e32 v210, 6, v35
	v_add3_u32 v215, v34, v209, v210
	v_max_f32_e32 v34, v3, v3
	v_max_f32_e32 v35, v2, v2
	v_max_f32_e32 v34, v35, v34
	v_max3_f32 v35, v4, v5, v19
	v_max3_f32 v34, v34, v18, v20
	v_max3_f32 v34, v34, v21, v6
	v_max3_f32 v35, v35, v8, v9
	v_max3_f32 v34, v34, v7, v22
	v_max3_f32 v35, v35, v24, v25
	v_max3_f32 v34, v34, v23, v10
	v_max3_f32 v35, v35, v12, v13
	v_max3_f32 v34, v34, v11, v26
	v_max3_f32 v35, v35, v28, v29
	v_max3_f32 v34, v34, v27, v14
	v_max3_f32 v35, v35, v16, v17
	v_max3_f32 v34, v34, v15, v30
	v_max3_f32 v35, v35, v32, v33
	v_max3_f32 v34, v34, v31, v35
	v_mov_b32_e32 v35, v34
	s_lshl_b64 s[16:17], s[0:1], 10
	s_and_b32 s0, s36, 0x3fffffc0
	v_permlane32_swap_b32_e32 v34, v35
	s_lshl_b32 s0, s0, 2
	v_max_f32_e32 v35, v35, v35
	v_max_f32_e32 v34, v34, v34
	s_add_i32 s0, s0, 0
	v_max_f32_e32 v34, v34, v35
	s_mov_b32 s47, 0x41000000
	s_add_i32 s30, s0, 0x18000
	v_cmp_le_f32_e32 vcc, -4.0, v34
	v_cmp_ge_f32_e64 s[0:1], s47, v34
	v_max_f32_e32 v34, 0xf149f2ca, v34
	s_and_b64 s[0:1], vcc, s[0:1]
	v_cndmask_b32_e64 v192, v34, 0, s[0:1]
	s_cmp_eq_u64 s[0:1], exec
	s_cbranch_scc1 .Lt0fast_1
	s_nop 0
	s_nop 0
	s_nop 0
	s_nop 0
	s_nop 0
	s_nop 0
	s_nop 0
	s_nop 0
	s_nop 0
	s_nop 0
	s_nop 0
	s_nop 0
	s_nop 0
	s_nop 0
	v_add_f32_e64 v2, v2, -v192
	v_exp_f32_e32 v50, v2
	v_add_f32_e64 v2, v18, -v192
	v_exp_f32_e32 v34, v2
	v_add_f32_e64 v2, v3, -v192
	v_exp_f32_e32 v51, v2
	v_add_f32_e64 v2, v19, -v192
	v_exp_f32_e32 v35, v2
	v_add_f32_e64 v2, v4, -v192
	v_exp_f32_e32 v52, v2
	v_add_f32_e64 v2, v20, -v192
	v_exp_f32_e32 v36, v2
	v_add_f32_e64 v2, v5, -v192
	v_exp_f32_e32 v53, v2
	v_add_f32_e64 v2, v21, -v192
	v_exp_f32_e32 v37, v2
	v_add_f32_e64 v2, v6, -v192
	v_exp_f32_e32 v54, v2
	v_add_f32_e64 v2, v22, -v192
	v_exp_f32_e32 v38, v2
	v_add_f32_e64 v2, v7, -v192
	v_exp_f32_e32 v55, v2
	v_add_f32_e64 v2, v23, -v192
	v_exp_f32_e32 v39, v2
	v_add_f32_e64 v2, v8, -v192
	v_exp_f32_e32 v56, v2
	v_add_f32_e64 v2, v24, -v192
	v_exp_f32_e32 v40, v2
	v_add_f32_e64 v2, v9, -v192
	v_exp_f32_e32 v57, v2
	v_add_f32_e64 v2, v25, -v192
	v_exp_f32_e32 v41, v2
	v_add_f32_e64 v2, v10, -v192
	v_exp_f32_e32 v58, v2
	v_add_f32_e64 v2, v26, -v192
	v_exp_f32_e32 v42, v2
	v_add_f32_e64 v2, v11, -v192
	v_exp_f32_e32 v59, v2
	v_add_f32_e64 v2, v27, -v192
	v_exp_f32_e32 v43, v2
	v_add_f32_e64 v2, v12, -v192
	v_exp_f32_e32 v60, v2
	v_add_f32_e64 v2, v28, -v192
	v_exp_f32_e32 v44, v2
	v_add_f32_e64 v2, v13, -v192
	v_exp_f32_e32 v61, v2
	v_add_f32_e64 v2, v29, -v192
	v_exp_f32_e32 v45, v2
	v_add_f32_e64 v2, v14, -v192
	v_exp_f32_e32 v62, v2
	v_add_f32_e64 v2, v30, -v192
	v_exp_f32_e32 v46, v2
	v_add_f32_e64 v2, v15, -v192
	v_exp_f32_e32 v63, v2
	v_add_f32_e64 v2, v31, -v192
	v_exp_f32_e32 v47, v2
	v_add_f32_e64 v2, v16, -v192
	v_exp_f32_e32 v64, v2
	v_add_f32_e64 v2, v32, -v192
	v_exp_f32_e32 v48, v2
	v_add_f32_e64 v2, v17, -v192
	v_exp_f32_e32 v65, v2
	v_add_f32_e64 v2, v33, -v192
.Lt0join_1:
	s_waitcnt vmcnt(0) lgkmcnt(0)
	s_barrier
	s_mov_b64 s[0:1], 0xc0000
	v_exp_f32_e32 v49, v2
	v_lshl_add_u64 v[2:3], v[194:195], 0, s[0:1]
	s_mov_b32 s0, m0
	s_mov_b32 m0, s41
	s_nop 0
	global_load_lds_dwordx4 v[2:3], off
	s_mov_b32 m0, s0
	s_mov_b64 s[0:1], 0xe0000
	v_lshl_add_u64 v[2:3], v[194:195], 0, s[0:1]
	s_mov_b32 s0, m0
	s_mov_b32 m0, s21
	s_nop 0
	global_load_lds_dwordx4 v[2:3], off
	s_mov_b32 m0, s0
	s_cmp_lg_u32 0, -1
	s_cselect_b32 s0, 0, 0
	s_add_i32 s0, s0, s20
	v_cmp_neq_f32_e32 vcc, 0, v192
	v_lshl_add_u64 v[2:3], v[196:197], 0, s[24:25]
	s_add_i32 s1, s0, 0x10000
	s_mov_b32 s20, m0
	s_mov_b32 m0, s1
	s_nop 0
	global_load_lds_dwordx4 v[2:3], off
	s_mov_b32 m0, s20
	s_add_i32 s0, s0, 0x12000
	v_lshl_add_u64 v[2:3], v[196:197], 0, s[26:27]
	s_mov_b32 s1, m0
	s_mov_b32 m0, s0
	s_nop 0
	global_load_lds_dwordx4 v[2:3], off
	s_mov_b32 m0, s1
	s_cmp_eq_u64 vcc, 0
	ds_read_b128 v[66:69], v70 offset:16384
	ds_read_b128 v[82:85], v70 offset:20480
	ds_read_b128 v[168:171], v71 offset:16384
	ds_read_b128 v[164:167], v71 offset:20480
	ds_read_b128 v[160:163], v72 offset:16384
	ds_read_b128 v[156:159], v72 offset:20480
	ds_read_b128 v[152:155], v73 offset:16384
	ds_read_b128 v[148:151], v73 offset:20480
	s_cselect_b64 s[20:21], -1, 0
	s_lshr_b32 s43, s36, 2
	s_and_b32 s43, s43, 0x3fffffc0
	s_add_u32 s43, s12, s43
	s_addc_u32 s49, s13, 0
	s_lshl_b32 s2, s2, 4
	v_and_b32_e32 v2, 3, v0
	s_lshl_b32 s3, s3, 7
	s_and_b32 s2, s2, 0x400
	v_lshlrev_b32_e32 v188, 4, v2
	v_add_lshl_u32 v4, s34, v1, 1
	s_or_b32 s34, s2, s3
	v_or_b32_e32 v2, s43, v188
	v_mov_b32_e32 v3, s49
	v_mov_b32_e32 v5, v189
	s_add_u32 s2, s8, s34
	v_lshl_add_u64 v[2:3], v[2:3], 0, v[4:5]
	s_addc_u32 s3, s9, 0
	s_waitcnt vmcnt(4) lgkmcnt(0)
	s_barrier
	v_lshl_add_u64 v[2:3], s[2:3], 0, v[2:3]
	v_mov_b32_e32 v18, v189
	v_mov_b32_e32 v19, v189
	v_lshl_add_u64 v[126:127], v[2:3], 0, s[28:29]
	v_mov_b32_e32 v20, v189
	v_mov_b32_e32 v21, v189
	v_mov_b32_e32 v22, v189
	v_mov_b32_e32 v23, v189
	v_mov_b32_e32 v24, v189
	v_mov_b32_e32 v25, v189
	v_mov_b32_e32 v26, v189
	v_mov_b32_e32 v27, v189
	v_mov_b32_e32 v28, v189
	v_mov_b32_e32 v29, v189
	v_mov_b32_e32 v30, v189
	v_mov_b32_e32 v31, v189
	v_mov_b32_e32 v32, v189
	v_mov_b32_e32 v33, v189
	v_mov_b64_e32 v[2:3], v[18:19]
	v_cmp_gt_u32_e64 s[0:1], 32, v212
	v_lshl_add_u32 v214, v202, 2, s30
	v_lshl_add_u32 v213, v201, 4, s30
	v_mov_b32_e32 v180, 0xff800000
	v_mov_b32_e32 v218, v189
	v_mov_b64_e32 v[4:5], v[20:21]
	v_mov_b64_e32 v[6:7], v[22:23]
	v_mov_b64_e32 v[8:9], v[24:25]
	v_mov_b64_e32 v[10:11], v[26:27]
	v_mov_b64_e32 v[12:13], v[28:29]
	v_mov_b64_e32 v[14:15], v[30:31]
	v_mov_b64_e32 v[16:17], v[32:33]

.LBB1_57:
	v_add_u32_e32 v0, s2, v191
	v_add3_u32 v197, v0, v209, v210
	v_max_f32_e32 v0, v33, v33
	v_max_f32_e32 v2, v32, v32
	v_max_f32_e32 v0, v2, v0
	v_max3_f32 v2, v34, v35, v17
	v_max3_f32 v0, v0, v16, v18
	v_max3_f32 v0, v0, v19, v36
	v_max3_f32 v2, v2, v38, v39
	v_max3_f32 v0, v0, v37, v20
	v_max3_f32 v2, v2, v22, v23
	v_max3_f32 v0, v0, v21, v40
	v_max3_f32 v2, v2, v42, v43
	v_max3_f32 v0, v0, v41, v24
	v_max3_f32 v2, v2, v26, v27
	v_max3_f32 v0, v0, v25, v44
	v_max3_f32 v2, v2, v46, v47
	v_max3_f32 v0, v0, v45, v28
	v_max3_f32 v2, v2, v30, v31
	v_max3_f32 v0, v0, v29, v2
	v_mov_b32_e32 v2, v0
	s_and_b32 s3, s23, 0x3fffffc0
	s_nop 0
	v_permlane32_swap_b32_e32 v0, v2
	s_lshl_b32 s2, s3, 2
	v_max_f32_e32 v2, v2, v2
	v_max_f32_e32 v0, v0, v0
	s_add_i32 s27, s2, 0
	v_max_f32_e32 v0, v0, v2
	s_mov_b32 s2, 0x41000000
	v_cmp_le_f32_e32 vcc, -4.0, v0
	v_cmp_ge_f32_e64 s[2:3], s2, v0
	v_max_f32_e32 v0, 0xf149f2ca, v0
	s_and_b64 s[2:3], vcc, s[2:3]
	v_cndmask_b32_e64 v192, v0, 0, s[2:3]
	s_cmp_eq_u64 s[2:3], exec
	s_cbranch_scc1 .Lt0fast_2
	s_nop 0
	s_nop 0
	s_nop 0
	s_nop 0
	s_nop 0
	s_nop 0
	s_nop 0
	s_nop 0
	s_nop 0
	s_nop 0
	s_nop 0
	s_nop 0
	s_nop 0
	s_nop 0
	v_add_f32_e64 v0, v32, -v192
	v_exp_f32_e32 v64, v0
	v_add_f32_e64 v0, v16, -v192
	v_exp_f32_e32 v32, v0
	v_add_f32_e64 v0, v33, -v192
	v_exp_f32_e32 v65, v0
	v_add_f32_e64 v0, v17, -v192
	v_exp_f32_e32 v33, v0
	v_add_f32_e64 v0, v34, -v192
	v_exp_f32_e32 v66, v0
	v_add_f32_e64 v0, v18, -v192
	v_exp_f32_e32 v34, v0
	v_add_f32_e64 v0, v35, -v192
	v_exp_f32_e32 v67, v0
	v_add_f32_e64 v0, v19, -v192
	v_exp_f32_e32 v35, v0
	v_add_f32_e64 v0, v36, -v192
	v_exp_f32_e32 v68, v0
	v_add_f32_e64 v0, v20, -v192
	v_exp_f32_e32 v36, v0
	v_add_f32_e64 v0, v37, -v192
	v_exp_f32_e32 v69, v0
	v_add_f32_e64 v0, v21, -v192
	v_exp_f32_e32 v37, v0
	v_add_f32_e64 v0, v38, -v192
	v_exp_f32_e32 v70, v0
	v_add_f32_e64 v0, v22, -v192
	v_exp_f32_e32 v38, v0
	v_add_f32_e64 v0, v39, -v192
	v_exp_f32_e32 v71, v0
	v_add_f32_e64 v0, v23, -v192
	v_exp_f32_e32 v39, v0
	v_add_f32_e64 v0, v40, -v192
	v_exp_f32_e32 v72, v0
	v_add_f32_e64 v0, v24, -v192
	v_exp_f32_e32 v40, v0
	v_add_f32_e64 v0, v41, -v192
	v_exp_f32_e32 v73, v0
	v_add_f32_e64 v0, v25, -v192
	v_exp_f32_e32 v41, v0
	v_add_f32_e64 v0, v42, -v192
	v_exp_f32_e32 v74, v0
	v_add_f32_e64 v0, v26, -v192
	v_exp_f32_e32 v42, v0
	v_add_f32_e64 v0, v43, -v192
	v_exp_f32_e32 v75, v0
	v_add_f32_e64 v0, v27, -v192
	v_exp_f32_e32 v43, v0
	v_add_f32_e64 v0, v44, -v192
	v_exp_f32_e32 v76, v0
	v_add_f32_e64 v0, v28, -v192
	v_exp_f32_e32 v44, v0
	v_add_f32_e64 v0, v45, -v192
	v_exp_f32_e32 v77, v0
	v_add_f32_e64 v0, v29, -v192
	v_exp_f32_e32 v45, v0
	v_add_f32_e64 v0, v46, -v192
	v_exp_f32_e32 v78, v0
	v_add_f32_e64 v0, v30, -v192
	v_exp_f32_e32 v46, v0
	v_add_f32_e64 v0, v47, -v192
	v_exp_f32_e32 v79, v0
	v_add_f32_e64 v0, v31, -v192
	v_exp_f32_e32 v47, v0
.Lt0join_2:
	s_bitcmp1_b32 s36, 8
	s_cbranch_scc1 .Lu2w_g1
	s_waitcnt vmcnt(4) lgkmcnt(0)
	s_branch .Lu2w_done

.Lt0fast_1:
	v_exp_f32_e32 v50, v2
	v_exp_f32_e32 v34, v18
	v_exp_f32_e32 v51, v3
	v_exp_f32_e32 v35, v19
	v_exp_f32_e32 v52, v4
	v_exp_f32_e32 v36, v20
	v_exp_f32_e32 v53, v5
	v_exp_f32_e32 v37, v21
	v_exp_f32_e32 v54, v6
	v_exp_f32_e32 v38, v22
	v_exp_f32_e32 v55, v7
	v_exp_f32_e32 v39, v23
	v_exp_f32_e32 v56, v8
	v_exp_f32_e32 v40, v24
	v_exp_f32_e32 v57, v9
	v_exp_f32_e32 v41, v25
	v_exp_f32_e32 v58, v10
	v_exp_f32_e32 v42, v26
	v_exp_f32_e32 v59, v11
	v_exp_f32_e32 v43, v27
	v_exp_f32_e32 v60, v12
	v_exp_f32_e32 v44, v28
	v_exp_f32_e32 v61, v13
	v_exp_f32_e32 v45, v29
	v_exp_f32_e32 v62, v14
	v_exp_f32_e32 v46, v30
	v_exp_f32_e32 v63, v15
	v_exp_f32_e32 v47, v31
	v_exp_f32_e32 v64, v16
	v_exp_f32_e32 v48, v32
	v_exp_f32_e32 v65, v17
	v_mov_b32_e32 v2, v33
	s_branch .Lt0join_1
.Lt0fast_2:
	v_exp_f32_e32 v64, v32
	v_exp_f32_e32 v32, v16
	v_exp_f32_e32 v65, v33
	v_exp_f32_e32 v33, v17
	v_exp_f32_e32 v66, v34
	v_exp_f32_e32 v34, v18
	v_exp_f32_e32 v67, v35
	v_exp_f32_e32 v35, v19
	v_exp_f32_e32 v68, v36
	v_exp_f32_e32 v36, v20
	v_exp_f32_e32 v69, v37
	v_exp_f32_e32 v37, v21
	v_exp_f32_e32 v70, v38
	v_exp_f32_e32 v38, v22
	v_exp_f32_e32 v71, v39
	v_exp_f32_e32 v39, v23
	v_exp_f32_e32 v72, v40
	v_exp_f32_e32 v40, v24
	v_exp_f32_e32 v73, v41
	v_exp_f32_e32 v41, v25
	v_exp_f32_e32 v74, v42
	v_exp_f32_e32 v42, v26
	v_exp_f32_e32 v75, v43
	v_exp_f32_e32 v43, v27
	v_exp_f32_e32 v76, v44
	v_exp_f32_e32 v44, v28
	v_exp_f32_e32 v77, v45
	v_exp_f32_e32 v45, v29
	v_exp_f32_e32 v78, v46
	v_exp_f32_e32 v46, v30
	v_exp_f32_e32 v79, v47
	v_exp_f32_e32 v47, v31
	s_branch .Lt0join_2
